# speedup vs baseline: 1.0517x; 1.0517x over previous
.LBB1_4:
	v_add_u32_e32 v182, s19, v191
	v_add_u32_e32 v238, s19, v192
	ds_read_b128 v[178:181], v182 offset:32768
	ds_read_b128 v[194:197], v182 offset:34816
	ds_read_b128 v[198:201], v182 offset:36864
	ds_read_b128 v[202:205], v182 offset:38912
	ds_read_b128 v[206:209], v238
	ds_read_b128 v[210:213], v238 offset:2048
	ds_read_b128 v[214:217], v238 offset:4096
	ds_read_b128 v[218:221], v238 offset:6144
	ds_read_b128 v[222:225], v238 offset:8192
	ds_read_b128 v[226:229], v238 offset:10240
	ds_read_b128 v[230:233], v238 offset:12288
	ds_read_b128 v[234:237], v238 offset:14336
	s_min_u32 s21, s20, 29
	s_xor_b32 s19, s19, 0x10000
	v_add_u32_e32 v239, s19, v189
	s_waitcnt vmcnt(11)
	v_cvt_pk_bf16_f32 v13, v12, v13
	v_cvt_pk_bf16_f32 v12, v10, v11
	s_waitcnt vmcnt(10)
	v_cvt_pk_bf16_f32 v11, v20, v21
	v_cvt_pk_bf16_f32 v10, v18, v19
	ds_write2st64_b64 v239, v[12:13], v[10:11] offset1:8
	s_waitcnt vmcnt(9)
	v_cvt_pk_bf16_f32 v11, v24, v25
	v_cvt_pk_bf16_f32 v10, v22, v23
	s_waitcnt vmcnt(8)
	v_cvt_pk_bf16_f32 v13, v32, v33
	v_cvt_pk_bf16_f32 v12, v30, v31
	ds_write2st64_b64 v239, v[10:11], v[12:13] offset0:16 offset1:24
	s_waitcnt vmcnt(7)
	v_cvt_pk_bf16_f32 v11, v36, v37
	v_cvt_pk_bf16_f32 v10, v34, v35
	s_waitcnt vmcnt(6)
	v_cvt_pk_bf16_f32 v13, v40, v41
	v_cvt_pk_bf16_f32 v12, v38, v39
	ds_write2st64_b64 v239, v[10:11], v[12:13] offset0:32 offset1:40
	s_waitcnt vmcnt(5)
	v_cvt_pk_bf16_f32 v11, v44, v45
	v_cvt_pk_bf16_f32 v10, v42, v43
	s_waitcnt vmcnt(4)
	v_cvt_pk_bf16_f32 v13, v48, v49
	v_cvt_pk_bf16_f32 v12, v46, v47
	ds_write2st64_b64 v239, v[10:11], v[12:13] offset0:48 offset1:56
	s_waitcnt lgkmcnt(0)
	s_add_i32 s21, s21, 2
	s_barrier
	s_setprio 1
	s_waitcnt lgkmcnt(11)
	v_mfma_f32_16x16x32_bf16 v[174:177], v[178:181], v[206:209], v[174:177]
	s_lshl_b32 s22, s21, 1
	s_and_b32 s22, s22, 0x60
	s_add_i32 s22, s22, s12
	s_lshl_b32 s22, s22, 6
	v_mfma_f32_16x16x32_bf16 v[170:173], v[194:197], v[206:209], v[170:173]
	s_and_b32 s22, s22, 0x3f00
	s_or_b32 s22, s22, s13
	s_lshl_b32 s23, s21, 23
	s_lshl_b32 s22, s22, 9
	v_mfma_f32_16x16x32_bf16 v[158:161], v[198:201], v[206:209], v[158:161]
	s_and_b32 s23, s23, 0x7000000
	s_or_b32 s22, s22, s23
	s_lshl_b32 s23, s21, 8
	s_and_b32 s23, s23, 0x100
	s_or_b32 s22, s22, s23
	s_or_b32 s23, s22, 0x4000
	buffer_load_dwordx4 v[10:13], v1, s[4:7], s22 offen sc0 nt
	v_mfma_f32_16x16x32_bf16 v[142:145], v[202:205], v[206:209], v[142:145]
	s_waitcnt lgkmcnt(10)
	v_mfma_f32_16x16x32_bf16 v[166:169], v[178:181], v[210:213], v[166:169]
	v_mfma_f32_16x16x32_bf16 v[162:165], v[194:197], v[210:213], v[162:165]
	v_mfma_f32_16x16x32_bf16 v[146:149], v[198:201], v[210:213], v[146:149]
	buffer_load_dwordx4 v[18:21], v1, s[4:7], s23 offen sc0 nt
	s_or_b32 s23, s22, 0x8000
	v_mfma_f32_16x16x32_bf16 v[122:125], v[202:205], v[210:213], v[122:125]
	s_waitcnt lgkmcnt(9)
	v_mfma_f32_16x16x32_bf16 v[154:157], v[178:181], v[214:217], v[154:157]
	v_mfma_f32_16x16x32_bf16 v[150:153], v[194:197], v[214:217], v[150:153]
	v_mfma_f32_16x16x32_bf16 v[130:133], v[198:201], v[214:217], v[130:133]
	buffer_load_dwordx4 v[22:25], v1, s[4:7], s23 offen sc0 nt
	s_or_b32 s23, s22, 0xc000
	v_mfma_f32_16x16x32_bf16 v[106:109], v[202:205], v[214:217], v[106:109]
	s_waitcnt lgkmcnt(8)
	v_mfma_f32_16x16x32_bf16 v[138:141], v[178:181], v[218:221], v[138:141]
	v_mfma_f32_16x16x32_bf16 v[134:137], v[194:197], v[218:221], v[134:137]
	v_mfma_f32_16x16x32_bf16 v[114:117], v[198:201], v[218:221], v[114:117]
	buffer_load_dwordx4 v[30:33], v1, s[4:7], s23 offen sc0 nt
	s_or_b32 s23, s22, 0x10000
	v_mfma_f32_16x16x32_bf16 v[90:93], v[202:205], v[218:221], v[90:93]
	s_waitcnt lgkmcnt(7)
	v_mfma_f32_16x16x32_bf16 v[126:129], v[178:181], v[222:225], v[126:129]
	v_mfma_f32_16x16x32_bf16 v[118:121], v[194:197], v[222:225], v[118:121]
	v_mfma_f32_16x16x32_bf16 v[98:101], v[198:201], v[222:225], v[98:101]
	buffer_load_dwordx4 v[34:37], v1, s[4:7], s23 offen sc0 nt
	s_or_b32 s23, s22, 0x14000
	v_mfma_f32_16x16x32_bf16 v[74:77], v[202:205], v[222:225], v[74:77]
	s_waitcnt lgkmcnt(6)
	v_mfma_f32_16x16x32_bf16 v[110:113], v[178:181], v[226:229], v[110:113]
	v_mfma_f32_16x16x32_bf16 v[102:105], v[194:197], v[226:229], v[102:105]
	v_mfma_f32_16x16x32_bf16 v[82:85], v[198:201], v[226:229], v[82:85]
	buffer_load_dwordx4 v[38:41], v1, s[4:7], s23 offen sc0 nt
	s_or_b32 s23, s22, 0x18000
	s_or_b32 s22, s22, 0x1c000
	v_mfma_f32_16x16x32_bf16 v[62:65], v[202:205], v[226:229], v[62:65]
	s_waitcnt lgkmcnt(5)
	v_mfma_f32_16x16x32_bf16 v[94:97], v[178:181], v[230:233], v[94:97]
	v_mfma_f32_16x16x32_bf16 v[86:89], v[194:197], v[230:233], v[86:89]
	v_mfma_f32_16x16x32_bf16 v[70:73], v[198:201], v[230:233], v[70:73]
	buffer_load_dwordx4 v[42:45], v1, s[4:7], s23 offen sc0 nt
	v_mfma_f32_16x16x32_bf16 v[54:57], v[202:205], v[230:233], v[54:57]
	s_waitcnt lgkmcnt(4)
	v_mfma_f32_16x16x32_bf16 v[78:81], v[178:181], v[234:237], v[78:81]
	v_mfma_f32_16x16x32_bf16 v[66:69], v[194:197], v[234:237], v[66:69]
	v_mfma_f32_16x16x32_bf16 v[58:61], v[198:201], v[234:237], v[58:61]
	buffer_load_dwordx4 v[46:49], v1, s[4:7], s22 offen sc0 nt
	v_mfma_f32_16x16x32_bf16 v[50:53], v[202:205], v[234:237], v[50:53]
	s_setprio 0
	s_waitcnt lgkmcnt(0)
	s_barrier
	ds_read_b128 v[178:181], v182 offset:33792
	ds_read_b128 v[194:197], v182 offset:35840
	ds_read_b128 v[198:201], v182 offset:37888
	ds_read_b128 v[202:205], v182 offset:39936
	ds_read_b128 v[206:209], v238 offset:1024
	ds_read_b128 v[210:213], v238 offset:3072
	ds_read_b128 v[214:217], v238 offset:5120
	ds_read_b128 v[218:221], v238 offset:7168
	ds_read_b128 v[222:225], v238 offset:9216
	ds_read_b128 v[226:229], v238 offset:11264
	ds_read_b128 v[230:233], v238 offset:13312
	ds_read_b128 v[234:237], v238 offset:15360
	v_add_u32_e32 v182, s19, v190
	s_waitcnt vmcnt(11)
	ds_write_b128 v182, v[2:5] offset:32768
	s_waitcnt vmcnt(10)
	ds_write_b128 v182, v[6:9] offset:40960
	s_waitcnt vmcnt(9)
	ds_write_b128 v182, v[14:17] offset:49152
	s_waitcnt vmcnt(8)
	ds_write_b128 v182, v[26:29] offset:57344
	s_waitcnt lgkmcnt(0)
	s_barrier
	s_setprio 1
	s_waitcnt lgkmcnt(11)
	v_mfma_f32_16x16x32_bf16 v[174:177], v[178:181], v[206:209], v[174:177]
	s_lshl_b32 s21, s21, 7
	s_and_b32 s21, s21, 0x780
	s_or_b32 s21, s21, s14
	s_or_b32 s22, s21, 0x20000
	v_mfma_f32_16x16x32_bf16 v[170:173], v[194:197], v[206:209], v[170:173]
	v_mfma_f32_16x16x32_bf16 v[158:161], v[198:201], v[206:209], v[158:161]
	v_mfma_f32_16x16x32_bf16 v[142:145], v[202:205], v[206:209], v[142:145]
	s_waitcnt lgkmcnt(10)
	v_mfma_f32_16x16x32_bf16 v[166:169], v[178:181], v[210:213], v[166:169]
	v_mfma_f32_16x16x32_bf16 v[162:165], v[194:197], v[210:213], v[162:165]
	buffer_load_dwordx4 v[2:5], v188, s[0:3], s21 offen sc1
	v_mfma_f32_16x16x32_bf16 v[146:149], v[198:201], v[210:213], v[146:149]
	v_mfma_f32_16x16x32_bf16 v[122:125], v[202:205], v[210:213], v[122:125]
	s_waitcnt lgkmcnt(9)
	v_mfma_f32_16x16x32_bf16 v[154:157], v[178:181], v[214:217], v[154:157]
	v_mfma_f32_16x16x32_bf16 v[150:153], v[194:197], v[214:217], v[150:153]
	v_mfma_f32_16x16x32_bf16 v[130:133], v[198:201], v[214:217], v[130:133]
	v_mfma_f32_16x16x32_bf16 v[106:109], v[202:205], v[214:217], v[106:109]
	s_waitcnt lgkmcnt(8)
	v_mfma_f32_16x16x32_bf16 v[138:141], v[178:181], v[218:221], v[138:141]
	v_mfma_f32_16x16x32_bf16 v[134:137], v[194:197], v[218:221], v[134:137]
	buffer_load_dwordx4 v[6:9], v188, s[0:3], s22 offen sc1
	s_or_b32 s22, s21, 0x40000
	s_or_b32 s21, s21, 0x60000
	v_mfma_f32_16x16x32_bf16 v[114:117], v[198:201], v[218:221], v[114:117]
	v_mfma_f32_16x16x32_bf16 v[90:93], v[202:205], v[218:221], v[90:93]
	s_waitcnt lgkmcnt(7)
	v_mfma_f32_16x16x32_bf16 v[126:129], v[178:181], v[222:225], v[126:129]
	v_mfma_f32_16x16x32_bf16 v[118:121], v[194:197], v[222:225], v[118:121]
	v_mfma_f32_16x16x32_bf16 v[98:101], v[198:201], v[222:225], v[98:101]
	v_mfma_f32_16x16x32_bf16 v[74:77], v[202:205], v[222:225], v[74:77]
	s_waitcnt lgkmcnt(6)
	v_mfma_f32_16x16x32_bf16 v[110:113], v[178:181], v[226:229], v[110:113]
	v_mfma_f32_16x16x32_bf16 v[102:105], v[194:197], v[226:229], v[102:105]
	buffer_load_dwordx4 v[14:17], v188, s[0:3], s22 offen sc1
	v_mfma_f32_16x16x32_bf16 v[82:85], v[198:201], v[226:229], v[82:85]
	v_mfma_f32_16x16x32_bf16 v[62:65], v[202:205], v[226:229], v[62:65]
	s_waitcnt lgkmcnt(5)
	v_mfma_f32_16x16x32_bf16 v[94:97], v[178:181], v[230:233], v[94:97]
	v_mfma_f32_16x16x32_bf16 v[86:89], v[194:197], v[230:233], v[86:89]
	v_mfma_f32_16x16x32_bf16 v[70:73], v[198:201], v[230:233], v[70:73]
	v_mfma_f32_16x16x32_bf16 v[54:57], v[202:205], v[230:233], v[54:57]
	s_waitcnt lgkmcnt(4)
	v_mfma_f32_16x16x32_bf16 v[78:81], v[178:181], v[234:237], v[78:81]
	v_mfma_f32_16x16x32_bf16 v[66:69], v[194:197], v[234:237], v[66:69]
	buffer_load_dwordx4 v[26:29], v188, s[0:3], s21 offen sc1
	v_mfma_f32_16x16x32_bf16 v[58:61], v[198:201], v[234:237], v[58:61]
	v_mfma_f32_16x16x32_bf16 v[50:53], v[202:205], v[234:237], v[50:53]
	s_setprio 0
	s_and_b32 s21, s20, 15
	s_cmp_lg_u32 s21, 15
	s_cbranch_scc1 .LBB1_3
	s_and_b32 s21, s18, 32
	s_add_i32 s21, s21, s12
	s_lshl_b32 s21, s21, 6
	s_and_b32 s21, s21, 0x3f00
	v_add_lshl_u32 v182, v193, s21, 9
	v_lshl_add_u64 v[206:207], v[184:185], 0, v[182:183]
	v_add_co_u32_e32 v208, vcc, s8, v206
	s_nop 1
	v_addc_co_u32_e32 v209, vcc, 0, v207, vcc
	v_add_co_u32_e32 v210, vcc, s15, v206
	s_nop 1
	v_addc_co_u32_e32 v211, vcc, 0, v207, vcc
	v_add_co_u32_e32 v212, vcc, s9, v206
	s_nop 1
	v_addc_co_u32_e32 v213, vcc, 0, v207, vcc
	v_add_co_u32_e32 v214, vcc, s16, v206
	s_nop 1
	v_addc_co_u32_e32 v215, vcc, 0, v207, vcc
	v_add_co_u32_e32 v216, vcc, s10, v206
	s_nop 1
	v_addc_co_u32_e32 v217, vcc, 0, v207, vcc
	v_add_co_u32_e32 v218, vcc, s17, v206
	s_nop 1
	v_addc_co_u32_e32 v219, vcc, 0, v207, vcc
	v_add_co_u32_e32 v220, vcc, s11, v206
	s_nop 1
	v_addc_co_u32_e32 v221, vcc, 0, v207, vcc
	global_store_dwordx4 v[206:207], v[174:177], off
	global_store_dwordx4 v[206:207], v[170:173], off offset:64
	global_store_dwordx4 v[206:207], v[158:161], off offset:128
	global_store_dwordx4 v[206:207], v[142:145], off offset:192
	global_store_dwordx4 v[208:209], v[166:169], off
	global_store_dwordx4 v[208:209], v[162:165], off offset:64
	global_store_dwordx4 v[208:209], v[146:149], off offset:128
	global_store_dwordx4 v[208:209], v[122:125], off offset:192
	global_store_dwordx4 v[210:211], v[154:157], off
	global_store_dwordx4 v[210:211], v[150:153], off offset:64
	global_store_dwordx4 v[210:211], v[130:133], off offset:128
	global_store_dwordx4 v[210:211], v[106:109], off offset:192
	global_store_dwordx4 v[212:213], v[138:141], off
	global_store_dwordx4 v[212:213], v[134:137], off offset:64
	global_store_dwordx4 v[212:213], v[114:117], off offset:128
	global_store_dwordx4 v[212:213], v[90:93], off offset:192
	global_store_dwordx4 v[214:215], v[126:129], off
	global_store_dwordx4 v[214:215], v[118:121], off offset:64
	global_store_dwordx4 v[214:215], v[98:101], off offset:128
	global_store_dwordx4 v[214:215], v[74:77], off offset:192
	global_store_dwordx4 v[216:217], v[110:113], off
	global_store_dwordx4 v[216:217], v[102:105], off offset:64
	global_store_dwordx4 v[216:217], v[82:85], off offset:128
	global_store_dwordx4 v[216:217], v[62:65], off offset:192
	global_store_dwordx4 v[218:219], v[94:97], off
	global_store_dwordx4 v[218:219], v[86:89], off offset:64
	global_store_dwordx4 v[218:219], v[70:73], off offset:128
	global_store_dwordx4 v[218:219], v[54:57], off offset:192
	global_store_dwordx4 v[220:221], v[78:81], off
	global_store_dwordx4 v[220:221], v[66:69], off offset:64
	global_store_dwordx4 v[220:221], v[58:61], off offset:128
	global_store_dwordx4 v[220:221], v[50:53], off offset:192
.Lpd_tail:
	s_waitcnt lgkmcnt(0)
	s_barrier
	s_add_i32 s20, s20, 1
	s_add_i32 s18, s18, 2
	v_add_u32_e32 v182, s19, v191
	v_add_u32_e32 v238, s19, v192
	ds_read_b128 v[178:181], v182 offset:32768
	ds_read_b128 v[194:197], v182 offset:34816
	ds_read_b128 v[198:201], v182 offset:36864
	ds_read_b128 v[202:205], v182 offset:38912
	ds_read_b128 v[206:209], v238
	ds_read_b128 v[210:213], v238 offset:2048
	ds_read_b128 v[214:217], v238 offset:4096
	ds_read_b128 v[218:221], v238 offset:6144
	ds_read_b128 v[222:225], v238 offset:8192
	ds_read_b128 v[226:229], v238 offset:10240
	ds_read_b128 v[230:233], v238 offset:12288
	ds_read_b128 v[234:237], v238 offset:14336
	s_min_u32 s21, s20, 29
	s_xor_b32 s19, s19, 0x10000
	v_add_u32_e32 v239, s19, v189
	s_waitcnt vmcnt(43)
	v_cvt_pk_bf16_f32 v13, v12, v13
	v_cvt_pk_bf16_f32 v12, v10, v11
	s_waitcnt vmcnt(42)
	v_cvt_pk_bf16_f32 v11, v20, v21
	v_cvt_pk_bf16_f32 v10, v18, v19
	ds_write2st64_b64 v239, v[12:13], v[10:11] offset1:8
	s_waitcnt vmcnt(41)
	v_cvt_pk_bf16_f32 v11, v24, v25
	v_cvt_pk_bf16_f32 v10, v22, v23
	s_waitcnt vmcnt(40)
	v_cvt_pk_bf16_f32 v13, v32, v33
	v_cvt_pk_bf16_f32 v12, v30, v31
	ds_write2st64_b64 v239, v[10:11], v[12:13] offset0:16 offset1:24
	s_waitcnt vmcnt(39)
	v_cvt_pk_bf16_f32 v11, v36, v37
	v_cvt_pk_bf16_f32 v10, v34, v35
	s_waitcnt vmcnt(38)
	v_cvt_pk_bf16_f32 v13, v40, v41
	v_cvt_pk_bf16_f32 v12, v38, v39
	ds_write2st64_b64 v239, v[10:11], v[12:13] offset0:32 offset1:40
	s_waitcnt vmcnt(37)
	v_cvt_pk_bf16_f32 v11, v44, v45
	v_cvt_pk_bf16_f32 v10, v42, v43
	s_waitcnt vmcnt(36)
	v_cvt_pk_bf16_f32 v13, v48, v49
	v_cvt_pk_bf16_f32 v12, v46, v47
	ds_write2st64_b64 v239, v[10:11], v[12:13] offset0:48 offset1:56
	s_waitcnt lgkmcnt(0)
	s_add_i32 s21, s21, 2
	s_barrier
	s_setprio 1
	s_waitcnt lgkmcnt(11)
	v_mfma_f32_16x16x32_bf16 v[174:177], v[178:181], v[206:209], v[240:243]
	s_lshl_b32 s22, s21, 1
	s_and_b32 s22, s22, 0x60
	s_add_i32 s22, s22, s12
	s_lshl_b32 s22, s22, 6
	v_mfma_f32_16x16x32_bf16 v[170:173], v[194:197], v[206:209], v[244:247]
	s_and_b32 s22, s22, 0x3f00
	s_or_b32 s22, s22, s13
	s_lshl_b32 s23, s21, 23
	s_lshl_b32 s22, s22, 9
	v_mfma_f32_16x16x32_bf16 v[158:161], v[198:201], v[206:209], v[248:251]
	s_and_b32 s23, s23, 0x7000000
	s_or_b32 s22, s22, s23
	s_lshl_b32 s23, s21, 8
	s_and_b32 s23, s23, 0x100
	s_or_b32 s22, s22, s23
	s_or_b32 s23, s22, 0x4000
	buffer_load_dwordx4 v[10:13], v1, s[4:7], s22 offen sc0 nt
	v_mfma_f32_16x16x32_bf16 v[142:145], v[202:205], v[206:209], v[252:255]
	s_waitcnt lgkmcnt(10)
	v_mfma_f32_16x16x32_bf16 v[166:169], v[178:181], v[210:213], v[240:243]
	v_mfma_f32_16x16x32_bf16 v[162:165], v[194:197], v[210:213], v[244:247]
	v_mfma_f32_16x16x32_bf16 v[146:149], v[198:201], v[210:213], v[248:251]
	buffer_load_dwordx4 v[18:21], v1, s[4:7], s23 offen sc0 nt
	s_or_b32 s23, s22, 0x8000
	v_mfma_f32_16x16x32_bf16 v[122:125], v[202:205], v[210:213], v[252:255]
	s_waitcnt lgkmcnt(9)
	v_mfma_f32_16x16x32_bf16 v[154:157], v[178:181], v[214:217], v[240:243]
	v_mfma_f32_16x16x32_bf16 v[150:153], v[194:197], v[214:217], v[244:247]
	v_mfma_f32_16x16x32_bf16 v[130:133], v[198:201], v[214:217], v[248:251]
	buffer_load_dwordx4 v[22:25], v1, s[4:7], s23 offen sc0 nt
	s_or_b32 s23, s22, 0xc000
	v_mfma_f32_16x16x32_bf16 v[106:109], v[202:205], v[214:217], v[252:255]
	s_waitcnt lgkmcnt(8)
	v_mfma_f32_16x16x32_bf16 v[138:141], v[178:181], v[218:221], v[240:243]
	v_mfma_f32_16x16x32_bf16 v[134:137], v[194:197], v[218:221], v[244:247]
	v_mfma_f32_16x16x32_bf16 v[114:117], v[198:201], v[218:221], v[248:251]
	buffer_load_dwordx4 v[30:33], v1, s[4:7], s23 offen sc0 nt
	s_or_b32 s23, s22, 0x10000
	v_mfma_f32_16x16x32_bf16 v[90:93], v[202:205], v[218:221], v[252:255]
	s_waitcnt lgkmcnt(7)
	v_mfma_f32_16x16x32_bf16 v[126:129], v[178:181], v[222:225], v[240:243]
	v_mfma_f32_16x16x32_bf16 v[118:121], v[194:197], v[222:225], v[244:247]
	v_mfma_f32_16x16x32_bf16 v[98:101], v[198:201], v[222:225], v[248:251]
	buffer_load_dwordx4 v[34:37], v1, s[4:7], s23 offen sc0 nt
	s_or_b32 s23, s22, 0x14000
	v_mfma_f32_16x16x32_bf16 v[74:77], v[202:205], v[222:225], v[252:255]
	s_waitcnt lgkmcnt(6)
	v_mfma_f32_16x16x32_bf16 v[110:113], v[178:181], v[226:229], v[240:243]
	v_mfma_f32_16x16x32_bf16 v[102:105], v[194:197], v[226:229], v[244:247]
	v_mfma_f32_16x16x32_bf16 v[82:85], v[198:201], v[226:229], v[248:251]
	buffer_load_dwordx4 v[38:41], v1, s[4:7], s23 offen sc0 nt
	s_or_b32 s23, s22, 0x18000
	s_or_b32 s22, s22, 0x1c000
	v_mfma_f32_16x16x32_bf16 v[62:65], v[202:205], v[226:229], v[252:255]
	s_waitcnt lgkmcnt(5)
	v_mfma_f32_16x16x32_bf16 v[94:97], v[178:181], v[230:233], v[240:243]
	v_mfma_f32_16x16x32_bf16 v[86:89], v[194:197], v[230:233], v[244:247]
	v_mfma_f32_16x16x32_bf16 v[70:73], v[198:201], v[230:233], v[248:251]
	buffer_load_dwordx4 v[42:45], v1, s[4:7], s23 offen sc0 nt
	v_mfma_f32_16x16x32_bf16 v[54:57], v[202:205], v[230:233], v[252:255]
	s_waitcnt lgkmcnt(4)
	v_mfma_f32_16x16x32_bf16 v[78:81], v[178:181], v[234:237], v[240:243]
	v_mfma_f32_16x16x32_bf16 v[66:69], v[194:197], v[234:237], v[244:247]
	v_mfma_f32_16x16x32_bf16 v[58:61], v[198:201], v[234:237], v[248:251]
	buffer_load_dwordx4 v[46:49], v1, s[4:7], s22 offen sc0 nt
	v_mfma_f32_16x16x32_bf16 v[50:53], v[202:205], v[234:237], v[252:255]
	s_setprio 0
	s_waitcnt lgkmcnt(0)
	s_barrier
	ds_read_b128 v[178:181], v182 offset:33792
	ds_read_b128 v[194:197], v182 offset:35840
	ds_read_b128 v[198:201], v182 offset:37888
	ds_read_b128 v[202:205], v182 offset:39936
	ds_read_b128 v[206:209], v238 offset:1024
	ds_read_b128 v[210:213], v238 offset:3072
	ds_read_b128 v[214:217], v238 offset:5120
	ds_read_b128 v[218:221], v238 offset:7168
	ds_read_b128 v[222:225], v238 offset:9216
	ds_read_b128 v[226:229], v238 offset:11264
	ds_read_b128 v[230:233], v238 offset:13312
	ds_read_b128 v[234:237], v238 offset:15360
	v_add_u32_e32 v182, s19, v190
	s_waitcnt vmcnt(43)
	ds_write_b128 v182, v[2:5] offset:32768
	s_waitcnt vmcnt(42)
	ds_write_b128 v182, v[6:9] offset:40960
	s_waitcnt vmcnt(41)
	ds_write_b128 v182, v[14:17] offset:49152
	s_waitcnt vmcnt(40)
	ds_write_b128 v182, v[26:29] offset:57344
	s_waitcnt lgkmcnt(0)
	s_barrier
	s_setprio 1
	s_waitcnt lgkmcnt(11)
	v_mfma_f32_16x16x32_bf16 v[174:177], v[178:181], v[206:209], v[174:177]
	s_lshl_b32 s21, s21, 7
	s_and_b32 s21, s21, 0x780
	s_or_b32 s21, s21, s14
	s_or_b32 s22, s21, 0x20000
	v_mfma_f32_16x16x32_bf16 v[170:173], v[194:197], v[206:209], v[170:173]
	v_mfma_f32_16x16x32_bf16 v[158:161], v[198:201], v[206:209], v[158:161]
	v_mfma_f32_16x16x32_bf16 v[142:145], v[202:205], v[206:209], v[142:145]
	s_waitcnt lgkmcnt(10)
	v_mfma_f32_16x16x32_bf16 v[166:169], v[178:181], v[210:213], v[166:169]
	v_mfma_f32_16x16x32_bf16 v[162:165], v[194:197], v[210:213], v[162:165]
	buffer_load_dwordx4 v[2:5], v188, s[0:3], s21 offen sc1
	v_mfma_f32_16x16x32_bf16 v[146:149], v[198:201], v[210:213], v[146:149]
	v_mfma_f32_16x16x32_bf16 v[122:125], v[202:205], v[210:213], v[122:125]
	s_waitcnt lgkmcnt(9)
	v_mfma_f32_16x16x32_bf16 v[154:157], v[178:181], v[214:217], v[154:157]
	v_mfma_f32_16x16x32_bf16 v[150:153], v[194:197], v[214:217], v[150:153]
	v_mfma_f32_16x16x32_bf16 v[130:133], v[198:201], v[214:217], v[130:133]
	v_mfma_f32_16x16x32_bf16 v[106:109], v[202:205], v[214:217], v[106:109]
	s_waitcnt lgkmcnt(8)
	v_mfma_f32_16x16x32_bf16 v[138:141], v[178:181], v[218:221], v[138:141]
	v_mfma_f32_16x16x32_bf16 v[134:137], v[194:197], v[218:221], v[134:137]
	buffer_load_dwordx4 v[6:9], v188, s[0:3], s22 offen sc1
	s_or_b32 s22, s21, 0x40000
	s_or_b32 s21, s21, 0x60000
	v_mfma_f32_16x16x32_bf16 v[114:117], v[198:201], v[218:221], v[114:117]
	v_mfma_f32_16x16x32_bf16 v[90:93], v[202:205], v[218:221], v[90:93]
	s_waitcnt lgkmcnt(7)
	v_mfma_f32_16x16x32_bf16 v[126:129], v[178:181], v[222:225], v[126:129]
	v_mfma_f32_16x16x32_bf16 v[118:121], v[194:197], v[222:225], v[118:121]
	v_mfma_f32_16x16x32_bf16 v[98:101], v[198:201], v[222:225], v[98:101]
	v_mfma_f32_16x16x32_bf16 v[74:77], v[202:205], v[222:225], v[74:77]
	s_waitcnt lgkmcnt(6)
	v_mfma_f32_16x16x32_bf16 v[110:113], v[178:181], v[226:229], v[110:113]
	v_mfma_f32_16x16x32_bf16 v[102:105], v[194:197], v[226:229], v[102:105]
	buffer_load_dwordx4 v[14:17], v188, s[0:3], s22 offen sc1
	v_mfma_f32_16x16x32_bf16 v[82:85], v[198:201], v[226:229], v[82:85]
	v_mfma_f32_16x16x32_bf16 v[62:65], v[202:205], v[226:229], v[62:65]
	s_waitcnt lgkmcnt(5)
	v_mfma_f32_16x16x32_bf16 v[94:97], v[178:181], v[230:233], v[94:97]
	v_mfma_f32_16x16x32_bf16 v[86:89], v[194:197], v[230:233], v[86:89]
	v_mfma_f32_16x16x32_bf16 v[70:73], v[198:201], v[230:233], v[70:73]
	v_mfma_f32_16x16x32_bf16 v[54:57], v[202:205], v[230:233], v[54:57]
	s_waitcnt lgkmcnt(4)
	v_mfma_f32_16x16x32_bf16 v[78:81], v[178:181], v[234:237], v[78:81]
	v_mfma_f32_16x16x32_bf16 v[66:69], v[194:197], v[234:237], v[66:69]
	buffer_load_dwordx4 v[26:29], v188, s[0:3], s21 offen sc1
	v_mfma_f32_16x16x32_bf16 v[58:61], v[198:201], v[234:237], v[58:61]
	v_mfma_f32_16x16x32_bf16 v[50:53], v[202:205], v[234:237], v[50:53]
	s_setprio 0
	s_branch .LBB1_3
.Lt30:
	v_add_u32_e32 v182, s19, v191
	v_add_u32_e32 v238, s19, v192
	ds_read_b128 v[178:181], v182 offset:32768
	ds_read_b128 v[194:197], v182 offset:34816
	ds_read_b128 v[198:201], v182 offset:36864
	ds_read_b128 v[202:205], v182 offset:38912
	ds_read_b128 v[206:209], v238
	ds_read_b128 v[210:213], v238 offset:2048
	ds_read_b128 v[214:217], v238 offset:4096
	ds_read_b128 v[218:221], v238 offset:6144
	ds_read_b128 v[222:225], v238 offset:8192
	ds_read_b128 v[226:229], v238 offset:10240
	ds_read_b128 v[230:233], v238 offset:12288
	ds_read_b128 v[234:237], v238 offset:14336
	s_min_u32 s21, s20, 29
	s_xor_b32 s19, s19, 0x10000
	v_add_u32_e32 v239, s19, v189
	s_waitcnt vmcnt(11)
	v_cvt_pk_bf16_f32 v13, v12, v13
	v_cvt_pk_bf16_f32 v12, v10, v11
	s_waitcnt vmcnt(10)
	v_cvt_pk_bf16_f32 v11, v20, v21
	v_cvt_pk_bf16_f32 v10, v18, v19
	ds_write2st64_b64 v239, v[12:13], v[10:11] offset1:8
	s_waitcnt vmcnt(9)
	v_cvt_pk_bf16_f32 v11, v24, v25
	v_cvt_pk_bf16_f32 v10, v22, v23
	s_waitcnt vmcnt(8)
	v_cvt_pk_bf16_f32 v13, v32, v33
	v_cvt_pk_bf16_f32 v12, v30, v31
	ds_write2st64_b64 v239, v[10:11], v[12:13] offset0:16 offset1:24
	s_waitcnt vmcnt(7)
	v_cvt_pk_bf16_f32 v11, v36, v37
	v_cvt_pk_bf16_f32 v10, v34, v35
	s_waitcnt vmcnt(6)
	v_cvt_pk_bf16_f32 v13, v40, v41
	v_cvt_pk_bf16_f32 v12, v38, v39
	ds_write2st64_b64 v239, v[10:11], v[12:13] offset0:32 offset1:40
	s_waitcnt vmcnt(5)
	v_cvt_pk_bf16_f32 v11, v44, v45
	v_cvt_pk_bf16_f32 v10, v42, v43
	s_waitcnt vmcnt(4)
	v_cvt_pk_bf16_f32 v13, v48, v49
	v_cvt_pk_bf16_f32 v12, v46, v47
	ds_write2st64_b64 v239, v[10:11], v[12:13] offset0:48 offset1:56
	s_waitcnt lgkmcnt(0)
	s_add_i32 s21, s21, 2
	s_barrier
	s_setprio 1
	s_waitcnt lgkmcnt(11)
	v_mfma_f32_16x16x32_bf16 v[174:177], v[178:181], v[206:209], v[174:177]
	s_lshl_b32 s22, s21, 1
	s_and_b32 s22, s22, 0x60
	s_add_i32 s22, s22, s12
	s_lshl_b32 s22, s22, 6
	v_mfma_f32_16x16x32_bf16 v[170:173], v[194:197], v[206:209], v[170:173]
	s_and_b32 s22, s22, 0x3f00
	s_or_b32 s22, s22, s13
	s_lshl_b32 s23, s21, 23
	s_lshl_b32 s22, s22, 9
	v_mfma_f32_16x16x32_bf16 v[158:161], v[198:201], v[206:209], v[158:161]
	s_and_b32 s23, s23, 0x7000000
	s_or_b32 s22, s22, s23
	s_lshl_b32 s23, s21, 8
	s_and_b32 s23, s23, 0x100
	s_or_b32 s22, s22, s23
	s_or_b32 s23, s22, 0x4000
	v_mfma_f32_16x16x32_bf16 v[142:145], v[202:205], v[206:209], v[142:145]
	s_waitcnt lgkmcnt(10)
	v_mfma_f32_16x16x32_bf16 v[166:169], v[178:181], v[210:213], v[166:169]
	v_mfma_f32_16x16x32_bf16 v[162:165], v[194:197], v[210:213], v[162:165]
	v_mfma_f32_16x16x32_bf16 v[146:149], v[198:201], v[210:213], v[146:149]
	s_or_b32 s23, s22, 0x8000
	v_mfma_f32_16x16x32_bf16 v[122:125], v[202:205], v[210:213], v[122:125]
	s_waitcnt lgkmcnt(9)
	v_mfma_f32_16x16x32_bf16 v[154:157], v[178:181], v[214:217], v[154:157]
	v_mfma_f32_16x16x32_bf16 v[150:153], v[194:197], v[214:217], v[150:153]
	v_mfma_f32_16x16x32_bf16 v[130:133], v[198:201], v[214:217], v[130:133]
	s_or_b32 s23, s22, 0xc000
	v_mfma_f32_16x16x32_bf16 v[106:109], v[202:205], v[214:217], v[106:109]
	s_waitcnt lgkmcnt(8)
	v_mfma_f32_16x16x32_bf16 v[138:141], v[178:181], v[218:221], v[138:141]
	v_mfma_f32_16x16x32_bf16 v[134:137], v[194:197], v[218:221], v[134:137]
	v_mfma_f32_16x16x32_bf16 v[114:117], v[198:201], v[218:221], v[114:117]
	s_or_b32 s23, s22, 0x10000
	v_mfma_f32_16x16x32_bf16 v[90:93], v[202:205], v[218:221], v[90:93]
	s_waitcnt lgkmcnt(7)
	v_mfma_f32_16x16x32_bf16 v[126:129], v[178:181], v[222:225], v[126:129]
	v_mfma_f32_16x16x32_bf16 v[118:121], v[194:197], v[222:225], v[118:121]
	v_mfma_f32_16x16x32_bf16 v[98:101], v[198:201], v[222:225], v[98:101]
	s_or_b32 s23, s22, 0x14000
	v_mfma_f32_16x16x32_bf16 v[74:77], v[202:205], v[222:225], v[74:77]
	s_waitcnt lgkmcnt(6)
	v_mfma_f32_16x16x32_bf16 v[110:113], v[178:181], v[226:229], v[110:113]
	v_mfma_f32_16x16x32_bf16 v[102:105], v[194:197], v[226:229], v[102:105]
	v_mfma_f32_16x16x32_bf16 v[82:85], v[198:201], v[226:229], v[82:85]
	s_or_b32 s23, s22, 0x18000
	s_or_b32 s22, s22, 0x1c000
	v_mfma_f32_16x16x32_bf16 v[62:65], v[202:205], v[226:229], v[62:65]
	s_waitcnt lgkmcnt(5)
	v_mfma_f32_16x16x32_bf16 v[94:97], v[178:181], v[230:233], v[94:97]
	v_mfma_f32_16x16x32_bf16 v[86:89], v[194:197], v[230:233], v[86:89]
	v_mfma_f32_16x16x32_bf16 v[70:73], v[198:201], v[230:233], v[70:73]
	v_mfma_f32_16x16x32_bf16 v[54:57], v[202:205], v[230:233], v[54:57]
	s_waitcnt lgkmcnt(4)
	v_mfma_f32_16x16x32_bf16 v[78:81], v[178:181], v[234:237], v[78:81]
	v_mfma_f32_16x16x32_bf16 v[66:69], v[194:197], v[234:237], v[66:69]
	v_mfma_f32_16x16x32_bf16 v[58:61], v[198:201], v[234:237], v[58:61]
	v_mfma_f32_16x16x32_bf16 v[50:53], v[202:205], v[234:237], v[50:53]
	s_setprio 0
	s_waitcnt lgkmcnt(0)
	s_barrier
	ds_read_b128 v[178:181], v182 offset:33792
	ds_read_b128 v[194:197], v182 offset:35840
	ds_read_b128 v[198:201], v182 offset:37888
	ds_read_b128 v[202:205], v182 offset:39936
	ds_read_b128 v[206:209], v238 offset:1024
	ds_read_b128 v[210:213], v238 offset:3072
	ds_read_b128 v[214:217], v238 offset:5120
	ds_read_b128 v[218:221], v238 offset:7168
	ds_read_b128 v[222:225], v238 offset:9216
	ds_read_b128 v[226:229], v238 offset:11264
	ds_read_b128 v[230:233], v238 offset:13312
	ds_read_b128 v[234:237], v238 offset:15360
	v_add_u32_e32 v182, s19, v190
	s_waitcnt vmcnt(3)
	ds_write_b128 v182, v[2:5] offset:32768
	s_waitcnt vmcnt(2)
	ds_write_b128 v182, v[6:9] offset:40960
	s_waitcnt vmcnt(1)
	ds_write_b128 v182, v[14:17] offset:49152
	s_waitcnt vmcnt(0)
	ds_write_b128 v182, v[26:29] offset:57344
	s_waitcnt lgkmcnt(0)
	s_barrier
	s_setprio 1
	s_waitcnt lgkmcnt(11)
	v_mfma_f32_16x16x32_bf16 v[174:177], v[178:181], v[206:209], v[174:177]
	s_lshl_b32 s21, s21, 7
	s_and_b32 s21, s21, 0x780
	s_or_b32 s21, s21, s14
	s_or_b32 s22, s21, 0x20000
	v_mfma_f32_16x16x32_bf16 v[170:173], v[194:197], v[206:209], v[170:173]
	v_mfma_f32_16x16x32_bf16 v[158:161], v[198:201], v[206:209], v[158:161]
	v_mfma_f32_16x16x32_bf16 v[142:145], v[202:205], v[206:209], v[142:145]
	s_waitcnt lgkmcnt(10)
	v_mfma_f32_16x16x32_bf16 v[166:169], v[178:181], v[210:213], v[166:169]
	v_mfma_f32_16x16x32_bf16 v[162:165], v[194:197], v[210:213], v[162:165]
	v_mfma_f32_16x16x32_bf16 v[146:149], v[198:201], v[210:213], v[146:149]
	v_mfma_f32_16x16x32_bf16 v[122:125], v[202:205], v[210:213], v[122:125]
	s_waitcnt lgkmcnt(9)
	v_mfma_f32_16x16x32_bf16 v[154:157], v[178:181], v[214:217], v[154:157]
	v_mfma_f32_16x16x32_bf16 v[150:153], v[194:197], v[214:217], v[150:153]
	v_mfma_f32_16x16x32_bf16 v[130:133], v[198:201], v[214:217], v[130:133]
	v_mfma_f32_16x16x32_bf16 v[106:109], v[202:205], v[214:217], v[106:109]
	s_waitcnt lgkmcnt(8)
	v_mfma_f32_16x16x32_bf16 v[138:141], v[178:181], v[218:221], v[138:141]
	v_mfma_f32_16x16x32_bf16 v[134:137], v[194:197], v[218:221], v[134:137]
	s_or_b32 s22, s21, 0x40000
	s_or_b32 s21, s21, 0x60000
	v_mfma_f32_16x16x32_bf16 v[114:117], v[198:201], v[218:221], v[114:117]
	v_mfma_f32_16x16x32_bf16 v[90:93], v[202:205], v[218:221], v[90:93]
	s_waitcnt lgkmcnt(7)
	v_mfma_f32_16x16x32_bf16 v[126:129], v[178:181], v[222:225], v[126:129]
	v_mfma_f32_16x16x32_bf16 v[118:121], v[194:197], v[222:225], v[118:121]
	v_mfma_f32_16x16x32_bf16 v[98:101], v[198:201], v[222:225], v[98:101]
	v_mfma_f32_16x16x32_bf16 v[74:77], v[202:205], v[222:225], v[74:77]
	s_waitcnt lgkmcnt(6)
	v_mfma_f32_16x16x32_bf16 v[110:113], v[178:181], v[226:229], v[110:113]
	v_mfma_f32_16x16x32_bf16 v[102:105], v[194:197], v[226:229], v[102:105]
	v_mfma_f32_16x16x32_bf16 v[82:85], v[198:201], v[226:229], v[82:85]
	v_mfma_f32_16x16x32_bf16 v[62:65], v[202:205], v[226:229], v[62:65]
	s_waitcnt lgkmcnt(5)
	v_mfma_f32_16x16x32_bf16 v[94:97], v[178:181], v[230:233], v[94:97]
	v_mfma_f32_16x16x32_bf16 v[86:89], v[194:197], v[230:233], v[86:89]
	v_mfma_f32_16x16x32_bf16 v[70:73], v[198:201], v[230:233], v[70:73]
	v_mfma_f32_16x16x32_bf16 v[54:57], v[202:205], v[230:233], v[54:57]
	s_waitcnt lgkmcnt(4)
	v_mfma_f32_16x16x32_bf16 v[78:81], v[178:181], v[234:237], v[78:81]
	v_mfma_f32_16x16x32_bf16 v[66:69], v[194:197], v[234:237], v[66:69]
	v_mfma_f32_16x16x32_bf16 v[58:61], v[198:201], v[234:237], v[58:61]
	v_mfma_f32_16x16x32_bf16 v[50:53], v[202:205], v[234:237], v[50:53]
	s_setprio 0
	s_waitcnt lgkmcnt(0)
	s_barrier
	s_add_i32 s20, s20, 1
	s_add_i32 s18, s18, 2
	v_add_u32_e32 v182, s19, v191
	v_add_u32_e32 v238, s19, v192
	ds_read_b128 v[178:181], v182 offset:32768
	ds_read_b128 v[194:197], v182 offset:34816
	ds_read_b128 v[198:201], v182 offset:36864
	ds_read_b128 v[202:205], v182 offset:38912
	ds_read_b128 v[206:209], v238
	ds_read_b128 v[210:213], v238 offset:2048
	ds_read_b128 v[214:217], v238 offset:4096
	ds_read_b128 v[218:221], v238 offset:6144
	ds_read_b128 v[222:225], v238 offset:8192
	ds_read_b128 v[226:229], v238 offset:10240
	ds_read_b128 v[230:233], v238 offset:12288
	ds_read_b128 v[234:237], v238 offset:14336
	s_min_u32 s21, s20, 29
	s_xor_b32 s19, s19, 0x10000
	v_add_u32_e32 v239, s19, v189
	s_waitcnt lgkmcnt(0)
	s_add_i32 s21, s21, 2
	s_barrier
	s_setprio 1
	s_waitcnt lgkmcnt(11)
	v_mfma_f32_16x16x32_bf16 v[174:177], v[178:181], v[206:209], v[174:177]
	s_lshl_b32 s22, s21, 1
	s_and_b32 s22, s22, 0x60
	s_add_i32 s22, s22, s12
	s_lshl_b32 s22, s22, 6
	v_mfma_f32_16x16x32_bf16 v[170:173], v[194:197], v[206:209], v[170:173]
	s_and_b32 s22, s22, 0x3f00
	s_or_b32 s22, s22, s13
	s_lshl_b32 s23, s21, 23
	s_lshl_b32 s22, s22, 9
	v_mfma_f32_16x16x32_bf16 v[158:161], v[198:201], v[206:209], v[158:161]
	s_and_b32 s23, s23, 0x7000000
	s_or_b32 s22, s22, s23
	s_lshl_b32 s23, s21, 8
	s_and_b32 s23, s23, 0x100
	s_or_b32 s22, s22, s23
	s_or_b32 s23, s22, 0x4000
	v_mfma_f32_16x16x32_bf16 v[142:145], v[202:205], v[206:209], v[142:145]
	s_waitcnt lgkmcnt(10)
	v_mfma_f32_16x16x32_bf16 v[166:169], v[178:181], v[210:213], v[166:169]
	v_mfma_f32_16x16x32_bf16 v[162:165], v[194:197], v[210:213], v[162:165]
	v_mfma_f32_16x16x32_bf16 v[146:149], v[198:201], v[210:213], v[146:149]
	s_or_b32 s23, s22, 0x8000
	v_mfma_f32_16x16x32_bf16 v[122:125], v[202:205], v[210:213], v[122:125]
	s_waitcnt lgkmcnt(9)
	v_mfma_f32_16x16x32_bf16 v[154:157], v[178:181], v[214:217], v[154:157]
	v_mfma_f32_16x16x32_bf16 v[150:153], v[194:197], v[214:217], v[150:153]
	v_mfma_f32_16x16x32_bf16 v[130:133], v[198:201], v[214:217], v[130:133]
	s_or_b32 s23, s22, 0xc000
	v_mfma_f32_16x16x32_bf16 v[106:109], v[202:205], v[214:217], v[106:109]
	s_waitcnt lgkmcnt(8)
	v_mfma_f32_16x16x32_bf16 v[138:141], v[178:181], v[218:221], v[138:141]
	v_mfma_f32_16x16x32_bf16 v[134:137], v[194:197], v[218:221], v[134:137]
	v_mfma_f32_16x16x32_bf16 v[114:117], v[198:201], v[218:221], v[114:117]
	s_or_b32 s23, s22, 0x10000
	v_mfma_f32_16x16x32_bf16 v[90:93], v[202:205], v[218:221], v[90:93]
	s_waitcnt lgkmcnt(7)
	v_mfma_f32_16x16x32_bf16 v[126:129], v[178:181], v[222:225], v[126:129]
	v_mfma_f32_16x16x32_bf16 v[118:121], v[194:197], v[222:225], v[118:121]
	v_mfma_f32_16x16x32_bf16 v[98:101], v[198:201], v[222:225], v[98:101]
	s_or_b32 s23, s22, 0x14000
	v_mfma_f32_16x16x32_bf16 v[74:77], v[202:205], v[222:225], v[74:77]
	s_waitcnt lgkmcnt(6)
	v_mfma_f32_16x16x32_bf16 v[110:113], v[178:181], v[226:229], v[110:113]
	v_mfma_f32_16x16x32_bf16 v[102:105], v[194:197], v[226:229], v[102:105]
	v_mfma_f32_16x16x32_bf16 v[82:85], v[198:201], v[226:229], v[82:85]
	s_or_b32 s23, s22, 0x18000
	s_or_b32 s22, s22, 0x1c000
	v_mfma_f32_16x16x32_bf16 v[62:65], v[202:205], v[226:229], v[62:65]
	s_waitcnt lgkmcnt(5)
	v_mfma_f32_16x16x32_bf16 v[94:97], v[178:181], v[230:233], v[94:97]
	v_mfma_f32_16x16x32_bf16 v[86:89], v[194:197], v[230:233], v[86:89]
	v_mfma_f32_16x16x32_bf16 v[70:73], v[198:201], v[230:233], v[70:73]
	v_mfma_f32_16x16x32_bf16 v[54:57], v[202:205], v[230:233], v[54:57]
	s_waitcnt lgkmcnt(4)
	v_mfma_f32_16x16x32_bf16 v[78:81], v[178:181], v[234:237], v[78:81]
	v_mfma_f32_16x16x32_bf16 v[66:69], v[194:197], v[234:237], v[66:69]
	v_mfma_f32_16x16x32_bf16 v[58:61], v[198:201], v[234:237], v[58:61]
	v_mfma_f32_16x16x32_bf16 v[50:53], v[202:205], v[234:237], v[50:53]
	s_setprio 0
	s_waitcnt lgkmcnt(0)
	s_barrier
	ds_read_b128 v[178:181], v182 offset:33792
	ds_read_b128 v[194:197], v182 offset:35840
	ds_read_b128 v[198:201], v182 offset:37888
	ds_read_b128 v[202:205], v182 offset:39936
	ds_read_b128 v[206:209], v238 offset:1024
	ds_read_b128 v[210:213], v238 offset:3072
	ds_read_b128 v[214:217], v238 offset:5120
	ds_read_b128 v[218:221], v238 offset:7168
	ds_read_b128 v[222:225], v238 offset:9216
	ds_read_b128 v[226:229], v238 offset:11264
	ds_read_b128 v[230:233], v238 offset:13312
	ds_read_b128 v[234:237], v238 offset:15360
	s_waitcnt lgkmcnt(0)
	s_barrier
	s_setprio 1
	s_waitcnt lgkmcnt(11)
	v_mfma_f32_16x16x32_bf16 v[174:177], v[178:181], v[206:209], v[174:177]
	s_lshl_b32 s21, s21, 7
	s_and_b32 s21, s21, 0x780
	s_or_b32 s21, s21, s14
	s_or_b32 s22, s21, 0x20000
	v_mfma_f32_16x16x32_bf16 v[170:173], v[194:197], v[206:209], v[170:173]
	v_mfma_f32_16x16x32_bf16 v[158:161], v[198:201], v[206:209], v[158:161]
	v_mfma_f32_16x16x32_bf16 v[142:145], v[202:205], v[206:209], v[142:145]
	s_waitcnt lgkmcnt(10)
	v_mfma_f32_16x16x32_bf16 v[166:169], v[178:181], v[210:213], v[166:169]
	v_mfma_f32_16x16x32_bf16 v[162:165], v[194:197], v[210:213], v[162:165]
	v_mfma_f32_16x16x32_bf16 v[146:149], v[198:201], v[210:213], v[146:149]
	v_mfma_f32_16x16x32_bf16 v[122:125], v[202:205], v[210:213], v[122:125]
	s_waitcnt lgkmcnt(9)
	v_mfma_f32_16x16x32_bf16 v[154:157], v[178:181], v[214:217], v[154:157]
	v_mfma_f32_16x16x32_bf16 v[150:153], v[194:197], v[214:217], v[150:153]
	v_mfma_f32_16x16x32_bf16 v[130:133], v[198:201], v[214:217], v[130:133]
	v_mfma_f32_16x16x32_bf16 v[106:109], v[202:205], v[214:217], v[106:109]
	s_waitcnt lgkmcnt(8)
	v_mfma_f32_16x16x32_bf16 v[138:141], v[178:181], v[218:221], v[138:141]
	v_mfma_f32_16x16x32_bf16 v[134:137], v[194:197], v[218:221], v[134:137]
	s_or_b32 s22, s21, 0x40000
	s_or_b32 s21, s21, 0x60000
	v_mfma_f32_16x16x32_bf16 v[114:117], v[198:201], v[218:221], v[114:117]
	v_mfma_f32_16x16x32_bf16 v[90:93], v[202:205], v[218:221], v[90:93]
	s_waitcnt lgkmcnt(7)
	v_mfma_f32_16x16x32_bf16 v[126:129], v[178:181], v[222:225], v[126:129]
	v_mfma_f32_16x16x32_bf16 v[118:121], v[194:197], v[222:225], v[118:121]
	v_mfma_f32_16x16x32_bf16 v[98:101], v[198:201], v[222:225], v[98:101]
	v_mfma_f32_16x16x32_bf16 v[74:77], v[202:205], v[222:225], v[74:77]
	s_waitcnt lgkmcnt(6)
	v_mfma_f32_16x16x32_bf16 v[110:113], v[178:181], v[226:229], v[110:113]
	v_mfma_f32_16x16x32_bf16 v[102:105], v[194:197], v[226:229], v[102:105]
	v_mfma_f32_16x16x32_bf16 v[82:85], v[198:201], v[226:229], v[82:85]
	v_mfma_f32_16x16x32_bf16 v[62:65], v[202:205], v[226:229], v[62:65]
	s_waitcnt lgkmcnt(5)
	v_mfma_f32_16x16x32_bf16 v[94:97], v[178:181], v[230:233], v[94:97]
	v_mfma_f32_16x16x32_bf16 v[86:89], v[194:197], v[230:233], v[86:89]
	v_mfma_f32_16x16x32_bf16 v[70:73], v[198:201], v[230:233], v[70:73]
	v_mfma_f32_16x16x32_bf16 v[54:57], v[202:205], v[230:233], v[54:57]
	s_waitcnt lgkmcnt(4)
	v_mfma_f32_16x16x32_bf16 v[78:81], v[178:181], v[234:237], v[78:81]
	v_mfma_f32_16x16x32_bf16 v[66:69], v[194:197], v[234:237], v[66:69]
	v_mfma_f32_16x16x32_bf16 v[58:61], v[198:201], v[234:237], v[58:61]
	v_mfma_f32_16x16x32_bf16 v[50:53], v[202:205], v[234:237], v[50:53]
	s_setprio 0
	s_and_b32 s21, s18, 32
	s_add_i32 s21, s21, s12
	s_lshl_b32 s21, s21, 6
	s_and_b32 s21, s21, 0x3f00
	v_add_lshl_u32 v182, v193, s21, 9
	v_lshl_add_u64 v[206:207], v[184:185], 0, v[182:183]
	v_add_co_u32_e32 v208, vcc, s8, v206
	s_nop 1
	v_addc_co_u32_e32 v209, vcc, 0, v207, vcc
	v_add_co_u32_e32 v210, vcc, s15, v206
	s_nop 1
	v_addc_co_u32_e32 v211, vcc, 0, v207, vcc
	v_add_co_u32_e32 v212, vcc, s9, v206
	s_nop 1
	v_addc_co_u32_e32 v213, vcc, 0, v207, vcc
	v_add_co_u32_e32 v214, vcc, s16, v206
	s_nop 1
	v_addc_co_u32_e32 v215, vcc, 0, v207, vcc
	v_add_co_u32_e32 v216, vcc, s10, v206
	s_nop 1
	v_addc_co_u32_e32 v217, vcc, 0, v207, vcc
	v_add_co_u32_e32 v218, vcc, s17, v206
	s_nop 1
	v_addc_co_u32_e32 v219, vcc, 0, v207, vcc
	v_add_co_u32_e32 v220, vcc, s11, v206
	s_nop 1
	v_addc_co_u32_e32 v221, vcc, 0, v207, vcc
	global_store_dwordx4 v[206:207], v[174:177], off
	global_store_dwordx4 v[206:207], v[170:173], off offset:64
	global_store_dwordx4 v[206:207], v[158:161], off offset:128
	global_store_dwordx4 v[206:207], v[142:145], off offset:192
	global_store_dwordx4 v[208:209], v[166:169], off
	global_store_dwordx4 v[208:209], v[162:165], off offset:64
	global_store_dwordx4 v[208:209], v[146:149], off offset:128
	global_store_dwordx4 v[208:209], v[122:125], off offset:192
	global_store_dwordx4 v[210:211], v[154:157], off
	global_store_dwordx4 v[210:211], v[150:153], off offset:64
	global_store_dwordx4 v[210:211], v[130:133], off offset:128
	global_store_dwordx4 v[210:211], v[106:109], off offset:192
	global_store_dwordx4 v[212:213], v[138:141], off
	global_store_dwordx4 v[212:213], v[134:137], off offset:64
	global_store_dwordx4 v[212:213], v[114:117], off offset:128
	global_store_dwordx4 v[212:213], v[90:93], off offset:192
	global_store_dwordx4 v[214:215], v[126:129], off
	global_store_dwordx4 v[214:215], v[118:121], off offset:64
	global_store_dwordx4 v[214:215], v[98:101], off offset:128
	global_store_dwordx4 v[214:215], v[74:77], off offset:192
	global_store_dwordx4 v[216:217], v[110:113], off
	global_store_dwordx4 v[216:217], v[102:105], off offset:64
	global_store_dwordx4 v[216:217], v[82:85], off offset:128
	global_store_dwordx4 v[216:217], v[62:65], off offset:192
	global_store_dwordx4 v[218:219], v[94:97], off
	global_store_dwordx4 v[218:219], v[86:89], off offset:64
	global_store_dwordx4 v[218:219], v[70:73], off offset:128
	global_store_dwordx4 v[218:219], v[54:57], off offset:192
	global_store_dwordx4 v[220:221], v[78:81], off
	global_store_dwordx4 v[220:221], v[66:69], off offset:64
	global_store_dwordx4 v[220:221], v[58:61], off offset:128
	global_store_dwordx4 v[220:221], v[50:53], off offset:192
	s_waitcnt lgkmcnt(0)
	s_barrier
	s_branch .LBB1_6
.Lfirst:
	v_add_u32_e32 v182, s19, v191
	v_add_u32_e32 v238, s19, v192
	ds_read_b128 v[178:181], v182 offset:32768
	ds_read_b128 v[194:197], v182 offset:34816
	ds_read_b128 v[198:201], v182 offset:36864
	ds_read_b128 v[202:205], v182 offset:38912
	ds_read_b128 v[206:209], v238
	ds_read_b128 v[210:213], v238 offset:2048
	ds_read_b128 v[214:217], v238 offset:4096
	ds_read_b128 v[218:221], v238 offset:6144
	ds_read_b128 v[222:225], v238 offset:8192
	ds_read_b128 v[226:229], v238 offset:10240
	ds_read_b128 v[230:233], v238 offset:12288
	ds_read_b128 v[234:237], v238 offset:14336
	s_min_u32 s21, s20, 29
	s_xor_b32 s19, s19, 0x10000
	v_add_u32_e32 v239, s19, v189
	s_waitcnt vmcnt(11)
	v_cvt_pk_bf16_f32 v13, v12, v13
	v_cvt_pk_bf16_f32 v12, v10, v11
	s_waitcnt vmcnt(10)
	v_cvt_pk_bf16_f32 v11, v20, v21
	v_cvt_pk_bf16_f32 v10, v18, v19
	ds_write2st64_b64 v239, v[12:13], v[10:11] offset1:8
	s_waitcnt vmcnt(9)
	v_cvt_pk_bf16_f32 v11, v24, v25
	v_cvt_pk_bf16_f32 v10, v22, v23
	s_waitcnt vmcnt(8)
	v_cvt_pk_bf16_f32 v13, v32, v33
	v_cvt_pk_bf16_f32 v12, v30, v31
	ds_write2st64_b64 v239, v[10:11], v[12:13] offset0:16 offset1:24
	s_waitcnt vmcnt(7)
	v_cvt_pk_bf16_f32 v11, v36, v37
	v_cvt_pk_bf16_f32 v10, v34, v35
	s_waitcnt vmcnt(6)
	v_cvt_pk_bf16_f32 v13, v40, v41
	v_cvt_pk_bf16_f32 v12, v38, v39
	ds_write2st64_b64 v239, v[10:11], v[12:13] offset0:32 offset1:40
	s_waitcnt vmcnt(5)
	v_cvt_pk_bf16_f32 v11, v44, v45
	v_cvt_pk_bf16_f32 v10, v42, v43
	s_waitcnt vmcnt(4)
	v_cvt_pk_bf16_f32 v13, v48, v49
	v_cvt_pk_bf16_f32 v12, v46, v47
	ds_write2st64_b64 v239, v[10:11], v[12:13] offset0:48 offset1:56
	s_waitcnt lgkmcnt(0)
	s_add_i32 s21, s21, 2
	s_barrier
	s_setprio 1
	s_waitcnt lgkmcnt(11)
	v_mfma_f32_16x16x32_bf16 v[174:177], v[178:181], v[206:209], v[240:243]
	s_lshl_b32 s22, s21, 1
	s_and_b32 s22, s22, 0x60
	s_add_i32 s22, s22, s12
	s_lshl_b32 s22, s22, 6
	v_mfma_f32_16x16x32_bf16 v[170:173], v[194:197], v[206:209], v[244:247]
	s_and_b32 s22, s22, 0x3f00
	s_or_b32 s22, s22, s13
	s_lshl_b32 s23, s21, 23
	s_lshl_b32 s22, s22, 9
	v_mfma_f32_16x16x32_bf16 v[158:161], v[198:201], v[206:209], v[248:251]
	s_and_b32 s23, s23, 0x7000000
	s_or_b32 s22, s22, s23
	s_lshl_b32 s23, s21, 8
	s_and_b32 s23, s23, 0x100
	s_or_b32 s22, s22, s23
	s_or_b32 s23, s22, 0x4000
	buffer_load_dwordx4 v[10:13], v1, s[4:7], s22 offen sc0 nt
	v_mfma_f32_16x16x32_bf16 v[142:145], v[202:205], v[206:209], v[252:255]
	s_waitcnt lgkmcnt(10)
	v_mfma_f32_16x16x32_bf16 v[166:169], v[178:181], v[210:213], v[240:243]
	v_mfma_f32_16x16x32_bf16 v[162:165], v[194:197], v[210:213], v[244:247]
	v_mfma_f32_16x16x32_bf16 v[146:149], v[198:201], v[210:213], v[248:251]
	buffer_load_dwordx4 v[18:21], v1, s[4:7], s23 offen sc0 nt
	s_or_b32 s23, s22, 0x8000
	v_mfma_f32_16x16x32_bf16 v[122:125], v[202:205], v[210:213], v[252:255]
	s_waitcnt lgkmcnt(9)
	v_mfma_f32_16x16x32_bf16 v[154:157], v[178:181], v[214:217], v[240:243]
	v_mfma_f32_16x16x32_bf16 v[150:153], v[194:197], v[214:217], v[244:247]
	v_mfma_f32_16x16x32_bf16 v[130:133], v[198:201], v[214:217], v[248:251]
	buffer_load_dwordx4 v[22:25], v1, s[4:7], s23 offen sc0 nt
	s_or_b32 s23, s22, 0xc000
	v_mfma_f32_16x16x32_bf16 v[106:109], v[202:205], v[214:217], v[252:255]
	s_waitcnt lgkmcnt(8)
	v_mfma_f32_16x16x32_bf16 v[138:141], v[178:181], v[218:221], v[240:243]
	v_mfma_f32_16x16x32_bf16 v[134:137], v[194:197], v[218:221], v[244:247]
	v_mfma_f32_16x16x32_bf16 v[114:117], v[198:201], v[218:221], v[248:251]
	buffer_load_dwordx4 v[30:33], v1, s[4:7], s23 offen sc0 nt
	s_or_b32 s23, s22, 0x10000
	v_mfma_f32_16x16x32_bf16 v[90:93], v[202:205], v[218:221], v[252:255]
	s_waitcnt lgkmcnt(7)
	v_mfma_f32_16x16x32_bf16 v[126:129], v[178:181], v[222:225], v[240:243]
	v_mfma_f32_16x16x32_bf16 v[118:121], v[194:197], v[222:225], v[244:247]
	v_mfma_f32_16x16x32_bf16 v[98:101], v[198:201], v[222:225], v[248:251]
	buffer_load_dwordx4 v[34:37], v1, s[4:7], s23 offen sc0 nt
	s_or_b32 s23, s22, 0x14000
	v_mfma_f32_16x16x32_bf16 v[74:77], v[202:205], v[222:225], v[252:255]
	s_waitcnt lgkmcnt(6)
	v_mfma_f32_16x16x32_bf16 v[110:113], v[178:181], v[226:229], v[240:243]
	v_mfma_f32_16x16x32_bf16 v[102:105], v[194:197], v[226:229], v[244:247]
	v_mfma_f32_16x16x32_bf16 v[82:85], v[198:201], v[226:229], v[248:251]
	buffer_load_dwordx4 v[38:41], v1, s[4:7], s23 offen sc0 nt
	s_or_b32 s23, s22, 0x18000
	s_or_b32 s22, s22, 0x1c000
	v_mfma_f32_16x16x32_bf16 v[62:65], v[202:205], v[226:229], v[252:255]
	s_waitcnt lgkmcnt(5)
	v_mfma_f32_16x16x32_bf16 v[94:97], v[178:181], v[230:233], v[240:243]
	v_mfma_f32_16x16x32_bf16 v[86:89], v[194:197], v[230:233], v[244:247]
	v_mfma_f32_16x16x32_bf16 v[70:73], v[198:201], v[230:233], v[248:251]
	buffer_load_dwordx4 v[42:45], v1, s[4:7], s23 offen sc0 nt
	v_mfma_f32_16x16x32_bf16 v[54:57], v[202:205], v[230:233], v[252:255]
	s_waitcnt lgkmcnt(4)
	v_mfma_f32_16x16x32_bf16 v[78:81], v[178:181], v[234:237], v[240:243]
	v_mfma_f32_16x16x32_bf16 v[66:69], v[194:197], v[234:237], v[244:247]
	v_mfma_f32_16x16x32_bf16 v[58:61], v[198:201], v[234:237], v[248:251]
	buffer_load_dwordx4 v[46:49], v1, s[4:7], s22 offen sc0 nt
	v_mfma_f32_16x16x32_bf16 v[50:53], v[202:205], v[234:237], v[252:255]
	s_setprio 0
	s_waitcnt lgkmcnt(0)
	s_barrier
	ds_read_b128 v[178:181], v182 offset:33792
	ds_read_b128 v[194:197], v182 offset:35840
	ds_read_b128 v[198:201], v182 offset:37888
	ds_read_b128 v[202:205], v182 offset:39936
	ds_read_b128 v[206:209], v238 offset:1024
	ds_read_b128 v[210:213], v238 offset:3072
	ds_read_b128 v[214:217], v238 offset:5120
	ds_read_b128 v[218:221], v238 offset:7168
	ds_read_b128 v[222:225], v238 offset:9216
	ds_read_b128 v[226:229], v238 offset:11264
	ds_read_b128 v[230:233], v238 offset:13312
	ds_read_b128 v[234:237], v238 offset:15360
	v_add_u32_e32 v182, s19, v190
	s_waitcnt vmcnt(11)
	ds_write_b128 v182, v[2:5] offset:32768
	s_waitcnt vmcnt(10)
	ds_write_b128 v182, v[6:9] offset:40960
	s_waitcnt vmcnt(9)
	ds_write_b128 v182, v[14:17] offset:49152
	s_waitcnt vmcnt(8)
	ds_write_b128 v182, v[26:29] offset:57344
	s_waitcnt lgkmcnt(0)
	s_barrier
	s_setprio 1
	s_waitcnt lgkmcnt(11)
	v_mfma_f32_16x16x32_bf16 v[174:177], v[178:181], v[206:209], v[174:177]
	s_lshl_b32 s21, s21, 7
	s_and_b32 s21, s21, 0x780
	s_or_b32 s21, s21, s14
	s_or_b32 s22, s21, 0x20000
	v_mfma_f32_16x16x32_bf16 v[170:173], v[194:197], v[206:209], v[170:173]
	v_mfma_f32_16x16x32_bf16 v[158:161], v[198:201], v[206:209], v[158:161]
	v_mfma_f32_16x16x32_bf16 v[142:145], v[202:205], v[206:209], v[142:145]
	s_waitcnt lgkmcnt(10)
	v_mfma_f32_16x16x32_bf16 v[166:169], v[178:181], v[210:213], v[166:169]
	v_mfma_f32_16x16x32_bf16 v[162:165], v[194:197], v[210:213], v[162:165]
	buffer_load_dwordx4 v[2:5], v188, s[0:3], s21 offen sc1
	v_mfma_f32_16x16x32_bf16 v[146:149], v[198:201], v[210:213], v[146:149]
	v_mfma_f32_16x16x32_bf16 v[122:125], v[202:205], v[210:213], v[122:125]
	s_waitcnt lgkmcnt(9)
	v_mfma_f32_16x16x32_bf16 v[154:157], v[178:181], v[214:217], v[154:157]
	v_mfma_f32_16x16x32_bf16 v[150:153], v[194:197], v[214:217], v[150:153]
	v_mfma_f32_16x16x32_bf16 v[130:133], v[198:201], v[214:217], v[130:133]
	v_mfma_f32_16x16x32_bf16 v[106:109], v[202:205], v[214:217], v[106:109]
	s_waitcnt lgkmcnt(8)
	v_mfma_f32_16x16x32_bf16 v[138:141], v[178:181], v[218:221], v[138:141]
	v_mfma_f32_16x16x32_bf16 v[134:137], v[194:197], v[218:221], v[134:137]
	buffer_load_dwordx4 v[6:9], v188, s[0:3], s22 offen sc1
	s_or_b32 s22, s21, 0x40000
	s_or_b32 s21, s21, 0x60000
	v_mfma_f32_16x16x32_bf16 v[114:117], v[198:201], v[218:221], v[114:117]
	v_mfma_f32_16x16x32_bf16 v[90:93], v[202:205], v[218:221], v[90:93]
	s_waitcnt lgkmcnt(7)
	v_mfma_f32_16x16x32_bf16 v[126:129], v[178:181], v[222:225], v[126:129]
	v_mfma_f32_16x16x32_bf16 v[118:121], v[194:197], v[222:225], v[118:121]
	v_mfma_f32_16x16x32_bf16 v[98:101], v[198:201], v[222:225], v[98:101]
	v_mfma_f32_16x16x32_bf16 v[74:77], v[202:205], v[222:225], v[74:77]
	s_waitcnt lgkmcnt(6)
	v_mfma_f32_16x16x32_bf16 v[110:113], v[178:181], v[226:229], v[110:113]
	v_mfma_f32_16x16x32_bf16 v[102:105], v[194:197], v[226:229], v[102:105]
	buffer_load_dwordx4 v[14:17], v188, s[0:3], s22 offen sc1
	v_mfma_f32_16x16x32_bf16 v[82:85], v[198:201], v[226:229], v[82:85]
	v_mfma_f32_16x16x32_bf16 v[62:65], v[202:205], v[226:229], v[62:65]
	s_waitcnt lgkmcnt(5)
	v_mfma_f32_16x16x32_bf16 v[94:97], v[178:181], v[230:233], v[94:97]
	v_mfma_f32_16x16x32_bf16 v[86:89], v[194:197], v[230:233], v[86:89]
	v_mfma_f32_16x16x32_bf16 v[70:73], v[198:201], v[230:233], v[70:73]
	v_mfma_f32_16x16x32_bf16 v[54:57], v[202:205], v[230:233], v[54:57]
	s_waitcnt lgkmcnt(4)
	v_mfma_f32_16x16x32_bf16 v[78:81], v[178:181], v[234:237], v[78:81]
	v_mfma_f32_16x16x32_bf16 v[66:69], v[194:197], v[234:237], v[66:69]
	buffer_load_dwordx4 v[26:29], v188, s[0:3], s21 offen sc1
	v_mfma_f32_16x16x32_bf16 v[58:61], v[198:201], v[234:237], v[58:61]
	v_mfma_f32_16x16x32_bf16 v[50:53], v[202:205], v[234:237], v[50:53]
	s_setprio 0
	s_branch .LBB1_3
